# gb2: grid barrier (4 per-layer sites): XCD leaders wait on the global arrival counter reaching its target (no separate generation bump on the critical path); last leader releases its XCD before bumpin
# baseline (speedup 1.0000x reference)
; __device__ __forceinline__ unsigned xb_ld(unsigned* p)              { return __hip_atomic_load(p, __ATOMIC_RELAXED, __HIP_MEMORY_SCOPE_AGENT); }
; __device__ __forceinline__ unsigned xb_add(unsigned* p, unsigned v) { return __hip_atomic_fetch_add(p, v, __ATOMIC_RELAXED, __HIP_MEMORY_SCOPE_AGENT); }
; #define XB_SPIN(cond, bar) do { unsigned _sp = 0; while (cond) { __builtin_amdgcn_s_sleep(1); \
;     if ((++_sp & 255u) == 0u) { if (xb_ld(&(bar)[XB_TMO])) break; if (_sp > XB_SPIN_CAP) { atomicAdd(&(bar)[XB_TMO], 1u); break; } } } } while (0)
; __device__ __forceinline__ void xcd_barrier(const XcdBarrier& b) {
;     ...
;         const unsigned old = xb_add(&bar[XB_XSUB(bx_)], 1u);
;         const unsigned gen = old / nloc;
;         if (old + 1u == (gen + 1u) * nloc) {
;             __builtin_amdgcn_fence(__ATOMIC_RELEASE, "agent");
;             asm volatile("s_waitcnt vmcnt(0)" ::: "memory");
;             const unsigned og = xb_add(&bar[XB_TOP], 1u);
;             const unsigned tg = og / nx;
;             if (og + 1u == (tg + 1u) * nx) xb_add(&bar[XB_TOPGEN], 1u);
;             else XB_SPIN(xb_ld(&bar[XB_TOPGEN]) == tg, bar);
.LBB0_784:
	s_andn2_saveexec_b64 s[0:1], s[0:1]
	s_cbranch_execz .LBB0_800
	v_mov_b32_e32 v1, s38
	v_add_co_u32_e32 v2, vcc, 0x3000, v1
	v_mov_b32_e32 v1, s39
	buffer_wbl2 sc1
	s_waitcnt vmcnt(0)
	v_addc_co_u32_e32 v3, vcc, 0, v1, vcc
	flat_atomic_add v1, v[2:3], v249 offset:1024 sc0
	v_cvt_f32_u32_e32 v2, v0
	v_sub_u32_e32 v3, 0, v0
	s_mov_b64 s[6:7], -1
	v_rcp_iflag_f32_e32 v2, v2
	s_nop 0
	v_mul_f32_e32 v2, 0x4f7ffffe, v2
	v_cvt_u32_f32_e32 v2, v2
	v_mul_lo_u32 v3, v3, v2
	v_mul_hi_u32 v3, v2, v3
	v_add_u32_e32 v2, v2, v3
	s_waitcnt vmcnt(0) lgkmcnt(0)
	v_mul_hi_u32 v2, v1, v2
	v_mul_lo_u32 v3, v2, v0
	v_sub_u32_e32 v3, v1, v3
	v_cmp_ge_u32_e32 vcc, v3, v0
	v_add_u32_e32 v4, 1, v2
	s_nop 0
	v_cndmask_b32_e32 v2, v2, v4, vcc
	v_sub_u32_e32 v4, v3, v0
	v_cndmask_b32_e32 v3, v3, v4, vcc
	v_cmp_ge_u32_e32 vcc, v3, v0
	v_add_u32_e32 v3, 1, v2
	s_nop 0
	v_cndmask_b32_e32 v2, v2, v3, vcc
	v_add_u32_e32 v3, 1, v1
	v_mad_u64_u32 v[0:1], s[0:1], v0, v2, v[0:1]
	s_add_u32 s0, s38, 0x3500
	s_addc_u32 s1, s39, 0
	v_cmp_ne_u32_e32 vcc, v3, v0
	v_mov_b32_e32 v3, v0
	v_mov_b64_e32 v[0:1], s[0:1]
	s_and_saveexec_b64 s[4:5], vcc
	s_cbranch_execz .LBB0_797
	v_mov_b64_e32 v[0:1], s[0:1]
	global_load_dword v0, v[0:1], off offset:-256 sc1
	s_mov_b64 s[12:13], 0
	s_waitcnt vmcnt(0) lgkmcnt(0)
	v_cmp_lt_u32_e32 vcc, v0, v3
	s_and_saveexec_b64 s[10:11], vcc
	s_cbranch_execz .LBB0_796
	s_add_u32 s6, s38, 0x200
	s_addc_u32 s7, s39, 0
	s_mov_b32 s3, 1
	s_branch .LBB0_789

; __device__ __forceinline__ unsigned xb_ld(unsigned* p)              { return __hip_atomic_load(p, __ATOMIC_RELAXED, __HIP_MEMORY_SCOPE_AGENT); }
; __device__ __forceinline__ unsigned xb_add(unsigned* p, unsigned v) { return __hip_atomic_fetch_add(p, v, __ATOMIC_RELAXED, __HIP_MEMORY_SCOPE_AGENT); }
; #define XB_SPIN(cond, bar) do { unsigned _sp = 0; while (cond) { __builtin_amdgcn_s_sleep(1); \
;     if ((++_sp & 255u) == 0u) { if (xb_ld(&(bar)[XB_TMO])) break; if (_sp > XB_SPIN_CAP) { atomicAdd(&(bar)[XB_TMO], 1u); break; } } } } while (0)
; __device__ __forceinline__ void xcd_barrier(const XcdBarrier& b) {
;     ...
;             const unsigned og = xb_add(&bar[XB_TOP], 1u);
;             const unsigned tg = og / nx;
;             if (og + 1u == (tg + 1u) * nx) xb_add(&bar[XB_TOPGEN], 1u);
;             else XB_SPIN(xb_ld(&bar[XB_TOPGEN]) == tg, bar);
.LBB0_794:
	v_mov_b64_e32 v[0:1], s[0:1]
	global_load_dword v0, v[0:1], off offset:-256 sc1
	s_add_i32 s3, s3, 1
	s_or_b64 s[18:19], s[18:19], exec
	s_waitcnt vmcnt(0) lgkmcnt(0)
	v_cmp_ge_u32_e32 vcc, v0, v3
	s_orn2_b64 s[16:17], vcc, exec
	s_branch .LBB0_788

; __device__ __forceinline__ unsigned xb_ld(unsigned* p)              { return __hip_atomic_load(p, __ATOMIC_RELAXED, __HIP_MEMORY_SCOPE_AGENT); }
; __device__ __forceinline__ unsigned xb_add(unsigned* p, unsigned v) { return __hip_atomic_fetch_add(p, v, __ATOMIC_RELAXED, __HIP_MEMORY_SCOPE_AGENT); }
; #define XB_SPIN(cond, bar) do { unsigned _sp = 0; while (cond) { __builtin_amdgcn_s_sleep(1); \
;     if ((++_sp & 255u) == 0u) { if (xb_ld(&(bar)[XB_TMO])) break; if (_sp > XB_SPIN_CAP) { atomicAdd(&(bar)[XB_TMO], 1u); break; } } } } while (0)
; __device__ __forceinline__ void xcd_barrier(const XcdBarrier& b) {
;     ...
;             if (og + 1u == (tg + 1u) * nx) xb_add(&bar[XB_TOPGEN], 1u);
;             else XB_SPIN(xb_ld(&bar[XB_TOPGEN]) == tg, bar);
;             __builtin_amdgcn_fence(__ATOMIC_ACQUIRE, "agent");
;             xb_add(&bar[XB_XGEN(bx_)], 1u);
;             asm volatile("s_waitcnt vmcnt(0)" ::: "memory");
.LBB0_797:
	s_or_b64 exec, exec, s[4:5]
	s_add_i32 s64, s2, 0x900
	s_lshl_b64 s[0:1], s[64:65], 2
	s_add_u32 s0, s38, s0
	s_addc_u32 s1, s39, s1
	v_mov_b64_e32 v[2:3], s[0:1]
	s_waitcnt vmcnt(0) lgkmcnt(0)
	flat_atomic_add v[2:3], v249
	s_and_saveexec_b64 s[0:1], s[6:7]
	s_cbranch_execz .LBB0_799
	flat_atomic_add v[0:1], v249
.LBB0_799:
	s_or_b64 exec, exec, s[0:1]
	buffer_inv sc1
	s_waitcnt vmcnt(0)

; __device__ __forceinline__ unsigned xb_ld(unsigned* p)              { return __hip_atomic_load(p, __ATOMIC_RELAXED, __HIP_MEMORY_SCOPE_AGENT); }
; __device__ __forceinline__ unsigned xb_add(unsigned* p, unsigned v) { return __hip_atomic_fetch_add(p, v, __ATOMIC_RELAXED, __HIP_MEMORY_SCOPE_AGENT); }
; #define XB_SPIN(cond, bar) do { unsigned _sp = 0; while (cond) { __builtin_amdgcn_s_sleep(1); \
;     if ((++_sp & 255u) == 0u) { if (xb_ld(&(bar)[XB_TMO])) break; if (_sp > XB_SPIN_CAP) { atomicAdd(&(bar)[XB_TMO], 1u); break; } } } } while (0)
; __device__ __forceinline__ void xcd_barrier(const XcdBarrier& b) {
;     ...
;             const unsigned og = xb_add(&bar[XB_TOP], 1u);
;             const unsigned tg = og / nx;
;             if (og + 1u == (tg + 1u) * nx) xb_add(&bar[XB_TOPGEN], 1u);
;             else XB_SPIN(xb_ld(&bar[XB_TOPGEN]) == tg, bar);
.LBB0_1690:
	v_mov_b32_e32 v1, s38
	v_add_co_u32_e32 v2, vcc, 0x3000, v1
	v_mov_b32_e32 v1, s39
	buffer_wbl2 sc1
	s_waitcnt vmcnt(0)
	v_addc_co_u32_e32 v3, vcc, 0, v1, vcc
	flat_atomic_add v1, v[2:3], v249 offset:1024 sc0
	v_cvt_f32_u32_e32 v2, v0
	v_sub_u32_e32 v3, 0, v0
	s_mov_b64 s[6:7], -1
	v_rcp_iflag_f32_e32 v2, v2
	s_nop 0
	v_mul_f32_e32 v2, 0x4f7ffffe, v2
	v_cvt_u32_f32_e32 v2, v2
	v_mul_lo_u32 v3, v3, v2
	v_mul_hi_u32 v3, v2, v3
	v_add_u32_e32 v2, v2, v3
	s_waitcnt vmcnt(0) lgkmcnt(0)
	v_mul_hi_u32 v2, v1, v2
	v_mul_lo_u32 v3, v2, v0
	v_sub_u32_e32 v3, v1, v3
	v_cmp_ge_u32_e32 vcc, v3, v0
	v_add_u32_e32 v4, 1, v2
	s_nop 0
	v_cndmask_b32_e32 v2, v2, v4, vcc
	v_sub_u32_e32 v4, v3, v0
	v_cndmask_b32_e32 v3, v3, v4, vcc
	v_cmp_ge_u32_e32 vcc, v3, v0
	v_add_u32_e32 v3, 1, v2
	s_nop 0
	v_cndmask_b32_e32 v2, v2, v3, vcc
	v_add_u32_e32 v3, 1, v1
	v_mad_u64_u32 v[0:1], s[0:1], v0, v2, v[0:1]
	s_add_u32 s0, s38, 0x3500
	s_addc_u32 s1, s39, 0
	v_cmp_ne_u32_e32 vcc, v3, v0
	v_mov_b64_e32 v[0:1], s[0:1]
	s_and_saveexec_b64 s[4:5], vcc
	s_cbranch_execz .LBB0_1702
	v_mov_b64_e32 v[0:1], s[0:1]
	flat_load_dword v0, v[0:1] sc1
	s_mov_b64 s[12:13], 0
	s_waitcnt vmcnt(0) lgkmcnt(0)
	v_cmp_le_u32_e32 vcc, v0, v2
	s_and_saveexec_b64 s[10:11], vcc
	s_cbranch_execz .LBB0_1701
	s_add_u32 s6, s38, 0x200
	s_addc_u32 s7, s39, 0
	s_mov_b32 s3, 1
	s_branch .LBB0_1694

; __device__ __forceinline__ unsigned xb_ld(unsigned* p)              { return __hip_atomic_load(p, __ATOMIC_RELAXED, __HIP_MEMORY_SCOPE_AGENT); }
; __device__ __forceinline__ unsigned xb_add(unsigned* p, unsigned v) { return __hip_atomic_fetch_add(p, v, __ATOMIC_RELAXED, __HIP_MEMORY_SCOPE_AGENT); }
; #define XB_SPIN(cond, bar) do { unsigned _sp = 0; while (cond) { __builtin_amdgcn_s_sleep(1); \
;     if ((++_sp & 255u) == 0u) { if (xb_ld(&(bar)[XB_TMO])) break; if (_sp > XB_SPIN_CAP) { atomicAdd(&(bar)[XB_TMO], 1u); break; } } } } while (0)
; __device__ __forceinline__ void xcd_barrier(const XcdBarrier& b) {
;     ...
;             const unsigned og = xb_add(&bar[XB_TOP], 1u);
;             const unsigned tg = og / nx;
;             if (og + 1u == (tg + 1u) * nx) xb_add(&bar[XB_TOPGEN], 1u);
;             else XB_SPIN(xb_ld(&bar[XB_TOPGEN]) == tg, bar);
.LBB0_1699:
	v_mov_b64_e32 v[0:1], s[0:1]
	flat_load_dword v0, v[0:1] sc1
	s_add_i32 s3, s3, 1
	s_or_b64 s[18:19], s[18:19], exec
	s_waitcnt vmcnt(0) lgkmcnt(0)
	v_cmp_gt_u32_e32 vcc, v0, v2
	s_orn2_b64 s[16:17], vcc, exec
	s_branch .LBB0_1693
